# phase-2 RG-LRU units: next unit's eight UX row loads issued one unit ahead into v216-v247 (software prefetch), on top of the router-weight layout change
# speedup vs baseline: 1.0106x; 1.0035x over previous
; template <bool FINAL>
; __device__ __forceinline__ void lru_unit(const Args& a, unsigned char* lds_g, int b, int cidx, int blk, int tid, bf16x8_t (&wl)[2][2][4], int& wl_blk) {
;     ...
;         const int pos = tid >> 3, cg = tid & 7, ch0 = blk * 128 + cg * 16, p = p0 + pos;
;         float z[16];
; #pragma unroll
;         for (int q = 0; q < 4; ++q) { const f32x4 bv = *(const f32x4*)(a.in[I_CONVB] + ch0 + 4 * q); z[4 * q] = bv.x; z[4 * q + 1] = bv.y; z[4 * q + 2] = bv.z; z[4 * q + 3] = bv.w; }
;         v4u ua[4], ub[4]; float msk[4];
; #pragma unroll
;         for (int w4 = 0; w4 < 4; ++w4) { const int pp = p + w4 - 2; const bool ok = pp >= 0 && pp < seglen; const int ppc = ok ? pp : p;
;             const v4u* src = (const v4u*)(UX + (size_t)lru_pos_row(b, isctx, ppc) * 1024 + ch0); ua[w4] = src[0]; ub[w4] = src[1]; msk[w4] = ok ? 1.f : 0.f; }
; __device__ __forceinline__ void phase3(const Args& a, unsigned char* lds_g, int tid) {
;     ...
;     for (int u = blockIdx.x; u < 4 * 36 * 8; u += gridDim.x) { const int blk = u & 7, q = u >> 3; lru_unit<false>(a, lds_g, q / 36, q % 36, blk, tid, wl, wl_blk); }
.Lp2_plain:
	s_and_b32 s74, s41, 7
	s_lshl_b32 s74, s74, 8
	s_ashr_i32 s75, s41, 3
	s_mul_hi_i32 s76, s75, 0x38e38e39
	s_ashr_i32 s76, s76, 3
	s_mul_i32 s77, s76, 36
	s_sub_i32 s77, s75, s77
	s_lshl_b32 s78, s77, 6
	s_add_i32 s79, s78, 0xffffff00
	s_lshl_b32 s80, s76, 8
	s_lshl_b32 s81, s76, 11
	s_bitset1_b32 s81, 10
	s_cmp_lt_i32 s77, 4
	s_cselect_b32 s78, s78, s79
	s_movk_i32 s79, 0x800
	s_cselect_b32 s79, 0x100, s79
	s_cselect_b32 s80, s80, s81
	s_cselect_b64 s[88:89], -1, 0
	v_mbcnt_lo_u32_b32 v248, -1, 0
	v_mbcnt_hi_u32_b32 v248, -1, v248
	v_readfirstlane_b32 s81, v180
	s_andn2_b32 s81, s81, 63
	v_or_b32_e32 v216, s81, v248
	v_lshrrev_b32_e32 v216, 3, v216
	v_add_u32_e32 v216, s78, v216
	v_and_b32_e32 v217, 7, v248
	v_lshl_or_b32 v217, v217, 5, s74
	v_add_u32_e32 v220, -2, v216
	v_cmp_gt_u32_e64 s[90:91], s79, v220
	v_cndmask_b32_e64 v220, v216, v220, s[90:91]
	v_and_b32_e32 v218, 31, v220
	v_lshrrev_b32_e32 v219, 5, v220
	v_lshl_or_b32 v218, v218, 6, v219
	v_cndmask_b32_e64 v220, v218, v220, s[88:89]
	v_add_lshl_u32 v220, v220, s80, 11
	v_or_b32_e32 v220, v220, v217
	v_mov_b32_e32 v221, 0
	v_add_u32_e32 v228, -1, v216
	v_cmp_gt_u32_e64 s[90:91], s79, v228
	v_cndmask_b32_e64 v228, v216, v228, s[90:91]
	v_and_b32_e32 v218, 31, v228
	v_lshrrev_b32_e32 v219, 5, v228
	v_lshl_or_b32 v218, v218, 6, v219
	v_cndmask_b32_e64 v228, v218, v228, s[88:89]
	v_add_lshl_u32 v228, v228, s80, 11
	v_or_b32_e32 v228, v228, v217
	v_mov_b32_e32 v229, 0
	v_mov_b32_e32 v236, v216
	v_and_b32_e32 v218, 31, v236
	v_lshrrev_b32_e32 v219, 5, v236
	v_lshl_or_b32 v218, v218, 6, v219
	v_cndmask_b32_e64 v236, v218, v236, s[88:89]
	v_add_lshl_u32 v236, v236, s80, 11
	v_or_b32_e32 v236, v236, v217
	v_mov_b32_e32 v237, 0
	v_add_u32_e32 v244, 1, v216
	v_cmp_gt_u32_e64 s[90:91], s79, v244
	v_cndmask_b32_e64 v244, v216, v244, s[90:91]
	v_and_b32_e32 v218, 31, v244
	v_lshrrev_b32_e32 v219, 5, v244
	v_lshl_or_b32 v218, v218, 6, v219
	v_cndmask_b32_e64 v244, v218, v244, s[88:89]
	v_add_lshl_u32 v244, v244, s80, 11
	v_or_b32_e32 v244, v244, v217
	v_mov_b32_e32 v245, 0
	v_lshl_add_u64 v[220:221], v[220:221], 0, s[14:15]
	v_lshl_add_u64 v[228:229], v[228:229], 0, s[14:15]
	v_lshl_add_u64 v[236:237], v[236:237], 0, s[14:15]
	v_lshl_add_u64 v[244:245], v[244:245], 0, s[14:15]
	global_load_dwordx4 v[216:219], v[220:221], off offset:16
	s_nop 0
	global_load_dwordx4 v[220:223], v[220:221], off
	s_nop 0
	global_load_dwordx4 v[224:227], v[228:229], off offset:16
	s_nop 0
	global_load_dwordx4 v[228:231], v[228:229], off
	s_nop 0
	global_load_dwordx4 v[232:235], v[236:237], off offset:16
	s_nop 0
	global_load_dwordx4 v[236:239], v[236:237], off
	s_nop 0
	global_load_dwordx4 v[240:243], v[244:245], off offset:16
	s_nop 0
	global_load_dwordx4 v[244:247], v[244:245], off
	s_nop 0
	s_branch .LBB0_285

; template <bool FINAL>
; __device__ __forceinline__ void lru_unit(const Args& a, unsigned char* lds_g, int b, int cidx, int blk, int tid, bf16x8_t (&wl)[2][2][4], int& wl_blk) {
;     ...
;         for (int w4 = 0; w4 < 4; ++w4) { const int pp = p + w4 - 2; const bool ok = pp >= 0 && pp < seglen; const int ppc = ok ? pp : p;
;             const v4u* src = (const v4u*)(UX + (size_t)lru_pos_row(b, isctx, ppc) * 1024 + ch0); ua[w4] = src[0]; ub[w4] = src[1]; msk[w4] = ok ? 1.f : 0.f; }
.LBB0_291:
	v_lshlrev_b32_e32 v74, 1, v73
	v_mov_b32_e32 v75, v129
	v_ashrrev_i32_e32 v73, 31, v72
	v_lshl_add_u64 v[104:105], s[14:15], 0, v[74:75]
	v_lshlrev_b64 v[72:73], 11, v[72:73]
	v_lshl_add_u64 v[76:77], v[104:105], 0, v[72:73]
	v_cmp_lt_i32_e32 vcc, 0, v112
	v_cmp_ge_i32_e64 s[4:5], s44, v112
	s_and_b64 s[4:5], vcc, s[4:5]
	v_cndmask_b32_e64 v76, 0, 1, s[6:7]
	v_subbrev_co_u32_e64 v77, vcc, 0, v112, s[4:5]
	v_cmp_ne_u32_e64 s[8:9], 1, v76
	s_andn2_b64 vcc, exec, s[6:7]
	s_mov_b64 s[0:1], -1
	s_cbranch_vccnz .LBB0_293
	v_lshlrev_b32_e32 v76, 6, v77
	v_and_b32_e32 v76, 0x7c0, v76
	v_ashrrev_i32_e32 v78, 5, v77
	v_add3_u32 v76, v78, s45, v76
	s_mov_b64 s[0:1], 0

; template <bool FINAL>
; __device__ __forceinline__ void lru_unit(const Args& a, unsigned char* lds_g, int b, int cidx, int blk, int tid, bf16x8_t (&wl)[2][2][4], int& wl_blk) {
;     ...
;         for (int w4 = 0; w4 < 4; ++w4) { const int pp = p + w4 - 2; const bool ok = pp >= 0 && pp < seglen; const int ppc = ok ? pp : p;
;             const v4u* src = (const v4u*)(UX + (size_t)lru_pos_row(b, isctx, ppc) * 1024 + ch0); ua[w4] = src[0]; ub[w4] = src[1]; msk[w4] = ok ? 1.f : 0.f; }
.LBB0_295:
	v_ashrrev_i32_e32 v77, 31, v76
	v_lshlrev_b64 v[76:77], 11, v[76:77]
	v_lshl_add_u64 v[84:85], v[104:105], 0, v[76:77]
	s_and_b64 vcc, exec, s[8:9]
	s_mov_b64 s[0:1], -1
	s_cbranch_vccnz .LBB0_297
	v_lshlrev_b32_e32 v84, 6, v111
	v_and_b32_e32 v84, 0x7c0, v84
	v_ashrrev_i32_e32 v85, 5, v112
	v_add3_u32 v84, v85, s45, v84
	s_mov_b64 s[0:1], 0

; template <bool FINAL>
; __device__ __forceinline__ void lru_unit(const Args& a, unsigned char* lds_g, int b, int cidx, int blk, int tid, bf16x8_t (&wl)[2][2][4], int& wl_blk) {
;     ...
;         for (int w4 = 0; w4 < 4; ++w4) { const int pp = p + w4 - 2; const bool ok = pp >= 0 && pp < seglen; const int ppc = ok ? pp : p;
;             const v4u* src = (const v4u*)(UX + (size_t)lru_pos_row(b, isctx, ppc) * 1024 + ch0); ua[w4] = src[0]; ub[w4] = src[1]; msk[w4] = ok ? 1.f : 0.f; }
.LBB0_299:
	v_ashrrev_i32_e32 v85, 31, v84
	v_lshlrev_b64 v[84:85], 11, v[84:85]
	v_lshl_add_u64 v[100:101], v[104:105], 0, v[84:85]
	s_nop 0
	v_add_u32_e32 v107, 1, v112
	v_cmp_lt_i32_e32 vcc, -2, v112
	v_cmp_gt_i32_e64 s[6:7], s44, v107
	s_and_b64 s[6:7], vcc, s[6:7]
	s_and_b64 vcc, exec, s[8:9]
	v_cndmask_b32_e64 v107, v112, v107, s[6:7]
	s_mov_b64 s[0:1], -1
	s_cbranch_vccnz .LBB0_301
	v_lshlrev_b32_e32 v108, 6, v107
	v_and_b32_e32 v108, 0x7c0, v108
	v_ashrrev_i32_e32 v109, 5, v107
	v_add3_u32 v108, v109, s45, v108
	s_mov_b64 s[0:1], 0

; template <bool FINAL>
; __device__ __forceinline__ void lru_unit(const Args& a, unsigned char* lds_g, int b, int cidx, int blk, int tid, bf16x8_t (&wl)[2][2][4], int& wl_blk) {
;     ...
;         for (int w4 = 0; w4 < 4; ++w4) { const int pp = p + w4 - 2; const bool ok = pp >= 0 && pp < seglen; const int ppc = ok ? pp : p;
;             const v4u* src = (const v4u*)(UX + (size_t)lru_pos_row(b, isctx, ppc) * 1024 + ch0); ua[w4] = src[0]; ub[w4] = src[1]; msk[w4] = ok ? 1.f : 0.f; }
; #pragma unroll
;         for (int w4 = 0; w4 < 4; ++w4) { const float* cw = a.in[I_CONVW] + w4 * 1024 + ch0;
;             const unsigned uu[8] = {ua[w4].x, ua[w4].y, ua[w4].z, ua[w4].w, ub[w4].x, ub[w4].y, ub[w4].z, ub[w4].w};
; #pragma unroll
;             for (int q = 0; q < 4; ++q) { const f32x4 cv = *(const f32x4*)(cw + 4 * q) * msk[w4]; z[4 * q] += cv.x * bflo(uu[2 * q]); z[4 * q + 1] += cv.y * bfhi(uu[2 * q]); z[4 * q + 2] += cv.z * bflo(uu[2 * q + 1]); z[4 * q + 3] += cv.w * bfhi(uu[2 * q + 1]); } }
.LBB0_303:
	v_mov_b32_e32 v107, v129
	v_lshl_add_u64 v[126:127], s[60:61], 0, v[106:107]
	v_add_co_u32_e32 v152, vcc, s69, v126
	global_load_dwordx4 v[114:117], v106, s[60:61]
	global_load_dwordx4 v[118:121], v106, s[60:61] offset:16
	v_addc_co_u32_e32 v153, vcc, 0, v127, vcc
	global_load_dwordx4 v[122:125], v106, s[60:61] offset:48
	global_load_dwordx4 v[136:139], v106, s[60:61] offset:32
	global_load_dwordx4 v[140:143], v[152:153], off offset:-4096
	v_lshl_add_u64 v[106:107], v[126:127], 0, s[50:51]
	v_ashrrev_i32_e32 v109, 31, v108
	global_load_dwordx4 v[144:147], v[106:107], off offset:16
	global_load_dwordx4 v[148:151], v[106:107], off offset:32
	v_lshlrev_b64 v[172:173], 11, v[108:109]
	global_load_dwordx4 v[106:109], v[106:107], off offset:48
	v_lshl_add_u64 v[164:165], v[126:127], 0, s[54:55]
	global_load_dwordx4 v[152:155], v[152:153], off
	s_nop 0
	global_load_dwordx4 v[156:159], v[164:165], off offset:16
	global_load_dwordx4 v[160:163], v[164:165], off offset:48
	s_nop 0
	global_load_dwordx4 v[164:167], v[164:165], off offset:32
	v_lshl_add_u64 v[104:105], v[104:105], 0, v[172:173]
	v_add_co_u32_e32 v168, vcc, s72, v126
	s_nop 0
	v_addc_co_u32_e32 v169, vcc, 0, v127, vcc
	v_lshl_add_u64 v[126:127], v[126:127], 0, s[56:57]
	global_load_dwordx4 v[168:171], v[168:169], off
	s_nop 0
	global_load_dwordx4 v[176:179], v[126:127], off offset:16
	global_load_dwordx4 v[198:201], v[126:127], off offset:32
	global_load_dwordx4 v[202:205], v[126:127], off offset:48
	v_cndmask_b32_e64 v206, 0, 1.0, s[10:11]
	v_cmp_gt_u32_e32 vcc, s44, v112
	v_cndmask_b32_e64 v112, 0, 1.0, s[4:5]
	s_waitcnt vmcnt(0)
	v_mov_b64_e32 v[88:89], v[220:221]
	v_mov_b64_e32 v[90:91], v[222:223]
	v_mov_b64_e32 v[72:73], v[216:217]
	v_mov_b64_e32 v[74:75], v[218:219]
	v_mov_b64_e32 v[96:97], v[228:229]
	v_mov_b64_e32 v[98:99], v[230:231]
	v_mov_b64_e32 v[76:77], v[224:225]
	v_mov_b64_e32 v[78:79], v[226:227]
	v_mov_b64_e32 v[100:101], v[236:237]
	v_mov_b64_e32 v[102:103], v[238:239]
	v_mov_b64_e32 v[84:85], v[232:233]
	v_mov_b64_e32 v[86:87], v[234:235]
	v_mov_b64_e32 v[172:173], v[244:245]
	v_mov_b64_e32 v[174:175], v[246:247]
	v_mov_b64_e32 v[194:195], v[240:241]
	v_mov_b64_e32 v[196:197], v[242:243]
	s_add_i32 s73, s41, s101
	s_cmp_lt_i32 s73, s100
	s_cbranch_scc0 .Lp2pf_skip
	s_and_b32 s74, s73, 7
	s_lshl_b32 s74, s74, 8
	s_ashr_i32 s75, s73, 3
	s_mul_hi_i32 s76, s75, 0x38e38e39
	s_ashr_i32 s76, s76, 3
	s_mul_i32 s77, s76, 36
	s_sub_i32 s77, s75, s77
	s_lshl_b32 s78, s77, 6
	s_add_i32 s79, s78, 0xffffff00
	s_lshl_b32 s80, s76, 8
	s_lshl_b32 s81, s76, 11
	s_bitset1_b32 s81, 10
	s_cmp_lt_i32 s77, 4
	s_cselect_b32 s78, s78, s79
	s_movk_i32 s79, 0x800
	s_cselect_b32 s79, 0x100, s79
	s_cselect_b32 s80, s80, s81
	s_cselect_b64 s[88:89], -1, 0
	v_mbcnt_lo_u32_b32 v248, -1, 0
	v_mbcnt_hi_u32_b32 v248, -1, v248
	v_readfirstlane_b32 s81, v180
	s_andn2_b32 s81, s81, 63
	v_or_b32_e32 v216, s81, v248
	v_lshrrev_b32_e32 v216, 3, v216
	v_add_u32_e32 v216, s78, v216
	v_and_b32_e32 v217, 7, v248
	v_lshl_or_b32 v217, v217, 5, s74
	v_add_u32_e32 v220, -2, v216
	v_cmp_gt_u32_e64 s[90:91], s79, v220
	v_cndmask_b32_e64 v220, v216, v220, s[90:91]
	v_and_b32_e32 v218, 31, v220
	v_lshrrev_b32_e32 v219, 5, v220
	v_lshl_or_b32 v218, v218, 6, v219
	v_cndmask_b32_e64 v220, v218, v220, s[88:89]
	v_add_lshl_u32 v220, v220, s80, 11
	v_or_b32_e32 v220, v220, v217
	v_mov_b32_e32 v221, 0
	v_add_u32_e32 v228, -1, v216
	v_cmp_gt_u32_e64 s[90:91], s79, v228
	v_cndmask_b32_e64 v228, v216, v228, s[90:91]
	v_and_b32_e32 v218, 31, v228
	v_lshrrev_b32_e32 v219, 5, v228
	v_lshl_or_b32 v218, v218, 6, v219
	v_cndmask_b32_e64 v228, v218, v228, s[88:89]
	v_add_lshl_u32 v228, v228, s80, 11
	v_or_b32_e32 v228, v228, v217
	v_mov_b32_e32 v229, 0
	v_mov_b32_e32 v236, v216
	v_and_b32_e32 v218, 31, v236
	v_lshrrev_b32_e32 v219, 5, v236
	v_lshl_or_b32 v218, v218, 6, v219
	v_cndmask_b32_e64 v236, v218, v236, s[88:89]
	v_add_lshl_u32 v236, v236, s80, 11
	v_or_b32_e32 v236, v236, v217
	v_mov_b32_e32 v237, 0
	v_add_u32_e32 v244, 1, v216
	v_cmp_gt_u32_e64 s[90:91], s79, v244
	v_cndmask_b32_e64 v244, v216, v244, s[90:91]
	v_and_b32_e32 v218, 31, v244
	v_lshrrev_b32_e32 v219, 5, v244
	v_lshl_or_b32 v218, v218, 6, v219
	v_cndmask_b32_e64 v244, v218, v244, s[88:89]
	v_add_lshl_u32 v244, v244, s80, 11
	v_or_b32_e32 v244, v244, v217
	v_mov_b32_e32 v245, 0
	v_lshl_add_u64 v[220:221], v[220:221], 0, s[14:15]
	v_lshl_add_u64 v[228:229], v[228:229], 0, s[14:15]
	v_lshl_add_u64 v[236:237], v[236:237], 0, s[14:15]
	v_lshl_add_u64 v[244:245], v[244:245], 0, s[14:15]
	global_load_dwordx4 v[216:219], v[220:221], off offset:16
	s_nop 0
	global_load_dwordx4 v[220:223], v[220:221], off
	s_nop 0
	global_load_dwordx4 v[224:227], v[228:229], off offset:16
	s_nop 0
	global_load_dwordx4 v[228:231], v[228:229], off
	s_nop 0
	global_load_dwordx4 v[232:235], v[236:237], off offset:16
	s_nop 0
	global_load_dwordx4 v[236:239], v[236:237], off
	s_nop 0
	global_load_dwordx4 v[240:243], v[244:245], off offset:16
	s_nop 0
	global_load_dwordx4 v[244:247], v[244:245], off
	s_nop 0
; #define WG_BAR() do { asm volatile("s_waitcnt lgkmcnt(0)" ::: "memory"); __builtin_amdgcn_s_barrier(); asm volatile("" ::: "memory"); } while (0)
; __device__ __forceinline__ unsigned pk2(float lo, float hi) { return pg8::cvt_pk_bf16(lo, hi); }
; template <bool FINAL>
; __device__ __forceinline__ void lru_unit(const Args& a, unsigned char* lds_g, int b, int cidx, int blk, int tid, bf16x8_t (&wl)[2][2][4], int& wl_blk) {
;     ...
; #pragma unroll
;         for (int w4 = 0; w4 < 4; ++w4) { const float* cw = a.in[I_CONVW] + w4 * 1024 + ch0;
;             const unsigned uu[8] = {ua[w4].x, ua[w4].y, ua[w4].z, ua[w4].w, ub[w4].x, ub[w4].y, ub[w4].z, ub[w4].w};
; #pragma unroll
;             for (int q = 0; q < 4; ++q) { const f32x4 cv = *(const f32x4*)(cw + 4 * q) * msk[w4]; z[4 * q] += cv.x * bflo(uu[2 * q]); z[4 * q + 1] += cv.y * bfhi(uu[2 * q]); z[4 * q + 2] += cv.z * bflo(uu[2 * q + 1]); z[4 * q + 3] += cv.w * bfhi(uu[2 * q + 1]); } }
; #pragma unroll
;         for (int q = 0; q < 4; ++q) *(f32x4*)(zf + pos * 132 + cg * 16 + 4 * q) = (f32x4){z[4 * q], z[4 * q + 1], z[4 * q + 2], z[4 * q + 3]};
;         v4u o0, o1; o0.x = pk2(z[0], z[1]); o0.y = pk2(z[2], z[3]); o0.z = pk2(z[4], z[5]); o0.w = pk2(z[6], z[7]); o1.x = pk2(z[8], z[9]); o1.y = pk2(z[10], z[11]); o1.z = pk2(z[12], z[13]); o1.w = pk2(z[14], z[15]);
;         *(v4u*)(zb + pos * 136 + cg * 16) = o0; *(v4u*)(zb + pos * 136 + cg * 16 + 8) = o1;
;     }
;     WG_BAR();
.Lp2pf_skip:
	v_lshlrev_b32_e32 v210, 16, v88
	v_and_b32_e32 v211, 0xffff0000, v88
	v_lshlrev_b32_e32 v88, 16, v89
	v_and_b32_e32 v89, 0xffff0000, v89
	v_cndmask_b32_e64 v104, 0, 1.0, vcc
	v_lshlrev_b32_e32 v212, 16, v96
	v_and_b32_e32 v213, 0xffff0000, v96
	v_lshlrev_b32_e32 v96, 16, v97
	v_and_b32_e32 v97, 0xffff0000, v97
	v_lshlrev_b32_e32 v214, 16, v100
	v_and_b32_e32 v215, 0xffff0000, v100
	v_lshlrev_b32_e32 v100, 16, v101
	v_and_b32_e32 v101, 0xffff0000, v101
	v_cndmask_b32_e64 v208, 0, 1.0, s[6:7]
	v_cmp_ngt_f32_e32 vcc, s35, v131
	v_pk_mul_f32 v[116:117], v[206:207], v[116:117] op_sel_hi:[0,1]
	v_pk_mul_f32 v[114:115], v[206:207], v[114:115] op_sel_hi:[0,1]
	v_pk_fma_f32 v[88:89], v[116:117], v[88:89], v[94:95]
	v_pk_fma_f32 v[92:93], v[114:115], v[210:211], v[92:93]
	v_pk_mul_f32 v[126:127], v[206:207], v[138:139] op_sel_hi:[0,1]
	v_pk_mul_f32 v[94:95], v[112:113], v[142:143] op_sel_hi:[0,1]
	v_pk_mul_f32 v[114:115], v[112:113], v[140:141] op_sel_hi:[0,1]
	v_pk_mul_f32 v[116:117], v[112:113], v[146:147] op_sel_hi:[0,1]
	v_pk_mul_f32 v[138:139], v[112:113], v[144:145] op_sel_hi:[0,1]
	v_pk_mul_f32 v[140:141], v[112:113], v[150:151] op_sel_hi:[0,1]
	v_pk_mul_f32 v[142:143], v[112:113], v[148:149] op_sel_hi:[0,1]
	v_pk_mul_f32 v[108:109], v[112:113], v[108:109] op_sel_hi:[0,1]
	v_pk_mul_f32 v[106:107], v[112:113], v[106:107] op_sel_hi:[0,1]
	v_pk_mul_f32 v[112:113], v[104:105], v[154:155] op_sel_hi:[0,1]
	v_pk_fma_f32 v[88:89], v[94:95], v[96:97], v[88:89]
	v_pk_mul_f32 v[118:119], v[206:207], v[118:119] op_sel_hi:[0,1]
	v_pk_fma_f32 v[88:89], v[112:113], v[100:101], v[88:89]
	v_lshlrev_b32_e32 v100, 16, v90
	v_and_b32_e32 v101, 0xffff0000, v90
	v_pk_fma_f32 v[80:81], v[118:119], v[100:101], v[80:81]
	v_lshlrev_b32_e32 v100, 16, v98
	v_and_b32_e32 v101, 0xffff0000, v98
	v_pk_mul_f32 v[148:149], v[104:105], v[156:157] op_sel_hi:[0,1]
	v_pk_fma_f32 v[80:81], v[138:139], v[100:101], v[80:81]
	v_lshlrev_b32_e32 v100, 16, v102
	v_and_b32_e32 v101, 0xffff0000, v102
	v_pk_mul_f32 v[96:97], v[208:209], v[176:177] op_sel_hi:[0,1]
	v_pk_fma_f32 v[80:81], v[148:149], v[100:101], v[80:81]
	v_lshlrev_b32_e32 v100, 16, v174
	v_and_b32_e32 v101, 0xffff0000, v174
	v_pk_mul_f32 v[120:121], v[206:207], v[120:121] op_sel_hi:[0,1]
	v_pk_mul_f32 v[136:137], v[206:207], v[136:137] op_sel_hi:[0,1]
	v_pk_fma_f32 v[80:81], v[96:97], v[100:101], v[80:81]
	v_lshlrev_b32_e32 v90, 16, v91
	v_and_b32_e32 v91, 0xffff0000, v91
	v_lshlrev_b32_e32 v96, 16, v72
	v_and_b32_e32 v97, 0xffff0000, v72
	v_lshlrev_b32_e32 v72, 16, v73
	v_and_b32_e32 v73, 0xffff0000, v73
	v_pk_fma_f32 v[82:83], v[120:121], v[90:91], v[82:83]
	v_lshlrev_b32_e32 v90, 16, v99
	v_and_b32_e32 v91, 0xffff0000, v99
	v_pk_fma_f32 v[68:69], v[136:137], v[96:97], v[68:69]
	v_lshlrev_b32_e32 v96, 16, v76
	v_and_b32_e32 v97, 0xffff0000, v76
	v_pk_fma_f32 v[70:71], v[126:127], v[72:73], v[70:71]
	v_lshlrev_b32_e32 v72, 16, v77
	v_and_b32_e32 v73, 0xffff0000, v77
	v_pk_mul_f32 v[124:125], v[206:207], v[124:125] op_sel_hi:[0,1]
	v_pk_mul_f32 v[146:147], v[104:105], v[158:159] op_sel_hi:[0,1]
	v_pk_mul_f32 v[154:155], v[104:105], v[162:163] op_sel_hi:[0,1]
	v_pk_mul_f32 v[156:157], v[208:209], v[170:171] op_sel_hi:[0,1]
	v_lshlrev_b32_e32 v162, 16, v173
	v_and_b32_e32 v163, 0xffff0000, v173
	v_pk_fma_f32 v[82:83], v[116:117], v[90:91], v[82:83]
	v_lshlrev_b32_e32 v90, 16, v103
	v_and_b32_e32 v91, 0xffff0000, v103
	v_pk_fma_f32 v[68:69], v[142:143], v[96:97], v[68:69]
	v_lshlrev_b32_e32 v96, 16, v84
	v_and_b32_e32 v97, 0xffff0000, v84
	v_pk_fma_f32 v[70:71], v[140:141], v[72:73], v[70:71]
	v_lshlrev_b32_e32 v72, 16, v85
	v_and_b32_e32 v73, 0xffff0000, v85
	v_lshlrev_b32_e32 v84, 16, v74
	v_and_b32_e32 v85, 0xffff0000, v74
	v_lshlrev_b32_e32 v74, 16, v75
	v_and_b32_e32 v75, 0xffff0000, v75
	v_pk_mul_f32 v[122:123], v[206:207], v[122:123] op_sel_hi:[0,1]
	v_pk_mul_f32 v[150:151], v[104:105], v[166:167] op_sel_hi:[0,1]
	v_pk_fma_f32 v[94:95], v[156:157], v[162:163], v[88:89]
	v_pk_mul_f32 v[88:89], v[208:209], v[178:179] op_sel_hi:[0,1]
	v_pk_fma_f32 v[82:83], v[146:147], v[90:91], v[82:83]
	v_lshlrev_b32_e32 v90, 16, v175
	v_and_b32_e32 v91, 0xffff0000, v175
	v_pk_fma_f32 v[66:67], v[124:125], v[74:75], v[66:67]
	v_lshlrev_b32_e32 v74, 16, v79
	v_and_b32_e32 v75, 0xffff0000, v79
	v_pk_fma_f32 v[82:83], v[88:89], v[90:91], v[82:83]
	v_pk_mul_f32 v[88:89], v[208:209], v[200:201] op_sel_hi:[0,1]
	v_pk_fma_f32 v[70:71], v[150:151], v[72:73], v[70:71]
	v_lshlrev_b32_e32 v72, 16, v195
	v_and_b32_e32 v73, 0xffff0000, v195
	v_pk_fma_f32 v[64:65], v[122:123], v[84:85], v[64:65]
	v_lshlrev_b32_e32 v84, 16, v78
	v_and_b32_e32 v85, 0xffff0000, v78
	v_pk_fma_f32 v[66:67], v[108:109], v[74:75], v[66:67]
	v_lshlrev_b32_e32 v74, 16, v87
	v_and_b32_e32 v75, 0xffff0000, v87
	v_pk_mul_f32 v[144:145], v[104:105], v[152:153] op_sel_hi:[0,1]
	v_pk_mul_f32 v[152:153], v[104:105], v[164:165] op_sel_hi:[0,1]
	v_pk_mul_f32 v[104:105], v[104:105], v[160:161] op_sel_hi:[0,1]
	v_pk_fma_f32 v[70:71], v[88:89], v[72:73], v[70:71]
	v_pk_mul_f32 v[72:73], v[208:209], v[204:205] op_sel_hi:[0,1]
	v_pk_fma_f32 v[64:65], v[106:107], v[84:85], v[64:65]
	v_lshlrev_b32_e32 v84, 16, v86
	v_and_b32_e32 v85, 0xffff0000, v86
	v_pk_fma_f32 v[66:67], v[154:155], v[74:75], v[66:67]
	v_lshlrev_b32_e32 v74, 16, v197
	v_and_b32_e32 v75, 0xffff0000, v197
	v_pk_fma_f32 v[92:93], v[114:115], v[212:213], v[92:93]
	v_pk_mul_f32 v[76:77], v[208:209], v[202:203] op_sel_hi:[0,1]
	v_pk_fma_f32 v[64:65], v[104:105], v[84:85], v[64:65]
	v_lshlrev_b32_e32 v84, 16, v196
	v_and_b32_e32 v85, 0xffff0000, v196
	v_pk_fma_f32 v[66:67], v[72:73], v[74:75], v[66:67]
	v_mul_lo_u32 v72, v111, s33
	v_pk_mul_f32 v[158:159], v[208:209], v[168:169] op_sel_hi:[0,1]
	v_lshlrev_b32_e32 v160, 16, v172
	v_and_b32_e32 v161, 0xffff0000, v172
	v_pk_fma_f32 v[92:93], v[144:145], v[214:215], v[92:93]
	v_pk_mul_f32 v[90:91], v[208:209], v[198:199] op_sel_hi:[0,1]
	v_pk_fma_f32 v[68:69], v[152:153], v[96:97], v[68:69]
	v_lshlrev_b32_e32 v96, 16, v194
	v_and_b32_e32 v97, 0xffff0000, v194
	v_pk_fma_f32 v[64:65], v[76:77], v[84:85], v[64:65]
	v_add_u32_e32 v76, 0, v72
	v_pk_fma_f32 v[92:93], v[158:159], v[160:161], v[92:93]
	v_pk_fma_f32 v[68:69], v[90:91], v[96:97], v[68:69]
	v_lshl_add_u32 v72, v110, 2, v76
	ds_write_b128 v72, v[92:95]
	ds_write_b128 v72, v[80:83] offset:16
	ds_write_b128 v72, v[68:71] offset:32
	ds_write_b128 v72, v[64:67] offset:48
	v_cvt_pk_bf16_f32 v68, v68, v69
	v_cvt_pk_bf16_f32 v69, v70, v71
	v_cvt_pk_bf16_f32 v70, v64, v65
	v_lshlrev_b32_e32 v64, 8, v111
	v_sub_u32_e32 v64, v76, v64
	v_cvt_pk_bf16_f32 v72, v92, v93
	v_cvt_pk_bf16_f32 v73, v94, v95
	v_cvt_pk_bf16_f32 v74, v80, v81
	v_cvt_pk_bf16_f32 v75, v82, v83
	v_lshl_add_u32 v64, v110, 1, v64
	v_cvt_pk_bf16_f32 v71, v66, v67
	ds_write_b128 v64, v[72:75] offset:33792
	ds_write_b128 v64, v[68:71] offset:33808
	v_and_b32_e32 v64, 48, v189
	v_add_u32_e32 v92, 0, v64
	s_waitcnt lgkmcnt(0)
	s_barrier
; template <bool FINAL>
; __device__ __forceinline__ void lru_unit(const Args& a, unsigned char* lds_g, int b, int cidx, int blk, int tid, bf16x8_t (&wl)[2][2][4], int& wl_blk) {
;     ...
;     for (int ks = 0; ks < 4; ++ks) {
;         bf16x8_t af[4];
; #pragma unroll
;         for (int mt = 0; mt < 4; ++mt) af[mt] = *(const bf16x8_t*)(zb + (16 * mt + fr) * 136 + 32 * ks + 8 * fq);
; #pragma unroll
;         for (int d = 0; d < 2; ++d)
; #pragma unroll
;             for (int m = 0; m < 2; ++m) {
; #pragma unroll
;                 for (int mt = 0; mt < 4; ++mt) acc[d][m][mt] = __builtin_amdgcn_mfma_f32_16x16x32_bf16(af[mt], wl[d][m][ks], acc[d][m][mt], 0, 0, 0); }
;     }
	v_mad_u32_u24 v133, v188, s34, v92
	v_or_b32_e32 v93, 48, v189
	ds_read_b128 v[64:67], v133 offset:33792
	ds_read_b128 v[68:71], v133 offset:38144
	ds_read_b128 v[72:75], v133 offset:33856
	ds_read_b128 v[80:83], v133 offset:42496
	ds_read_b128 v[84:87], v133 offset:38208
	v_mad_u32_u24 v164, v93, s34, v92
	ds_read_b128 v[92:95], v133 offset:42560
	ds_read_b128 v[100:103], v164 offset:33792
	ds_read_b128 v[104:107], v164 offset:33856
	s_waitcnt lgkmcnt(7)
	v_mfma_f32_16x16x32_bf16 v[76:79], v[64:67], v[0:3], 0
	s_waitcnt lgkmcnt(6)
	v_mfma_f32_16x16x32_bf16 v[88:91], v[68:71], v[0:3], 0
	s_waitcnt lgkmcnt(4)
	v_mfma_f32_16x16x32_bf16 v[96:99], v[80:83], v[0:3], 0
	s_waitcnt lgkmcnt(1)
	v_mfma_f32_16x16x32_bf16 v[108:111], v[100:103], v[0:3], 0
	v_mfma_f32_16x16x32_bf16 v[112:115], v[64:67], v[16:19], 0
	v_mfma_f32_16x16x32_bf16 v[116:119], v[68:71], v[16:19], 0
	v_mfma_f32_16x16x32_bf16 v[120:123], v[80:83], v[16:19], 0
	v_mfma_f32_16x16x32_bf16 v[124:127], v[100:103], v[16:19], 0
	v_mfma_f32_16x16x32_bf16 v[136:139], v[64:67], v[32:35], 0
	v_mfma_f32_16x16x32_bf16 v[140:143], v[68:71], v[32:35], 0
	v_mfma_f32_16x16x32_bf16 v[144:147], v[80:83], v[32:35], 0
	v_mfma_f32_16x16x32_bf16 v[148:151], v[100:103], v[32:35], 0
	v_mfma_f32_16x16x32_bf16 v[64:67], v[64:67], v[48:51], 0
	v_mfma_f32_16x16x32_bf16 v[68:71], v[68:71], v[48:51], 0
	v_mfma_f32_16x16x32_bf16 v[80:83], v[80:83], v[48:51], 0
	v_mfma_f32_16x16x32_bf16 v[100:103], v[100:103], v[48:51], 0
	v_mfma_f32_16x16x32_bf16 v[76:79], v[72:75], v[4:7], v[76:79]
	v_mfma_f32_16x16x32_bf16 v[88:91], v[84:87], v[4:7], v[88:91]
	v_mfma_f32_16x16x32_bf16 v[96:99], v[92:95], v[4:7], v[96:99]
	s_waitcnt lgkmcnt(0)
	v_mfma_f32_16x16x32_bf16 v[108:111], v[104:107], v[4:7], v[108:111]
	v_mfma_f32_16x16x32_bf16 v[112:115], v[72:75], v[20:23], v[112:115]
	v_mfma_f32_16x16x32_bf16 v[116:119], v[84:87], v[20:23], v[116:119]
	v_mfma_f32_16x16x32_bf16 v[120:123], v[92:95], v[20:23], v[120:123]
	v_mfma_f32_16x16x32_bf16 v[124:127], v[104:107], v[20:23], v[124:127]
	v_mfma_f32_16x16x32_bf16 v[136:139], v[72:75], v[36:39], v[136:139]
	v_mfma_f32_16x16x32_bf16 v[140:143], v[84:87], v[36:39], v[140:143]
	v_mfma_f32_16x16x32_bf16 v[144:147], v[92:95], v[36:39], v[144:147]
	v_mfma_f32_16x16x32_bf16 v[148:151], v[104:107], v[36:39], v[148:151]
	v_mfma_f32_16x16x32_bf16 v[64:67], v[72:75], v[52:55], v[64:67]
	v_mfma_f32_16x16x32_bf16 v[68:71], v[84:87], v[52:55], v[68:71]
	ds_read_b128 v[84:87], v133 offset:33920
	ds_read_b128 v[152:155], v133 offset:33984
	v_mfma_f32_16x16x32_bf16 v[72:75], v[92:95], v[52:55], v[80:83]
	ds_read_b128 v[92:95], v133 offset:38272
	ds_read_b128 v[156:159], v133 offset:38336
	v_mfma_f32_16x16x32_bf16 v[80:83], v[104:107], v[52:55], v[100:103]
	s_nop 2
	ds_read_b128 v[100:103], v133 offset:42624
	ds_read_b128 v[160:163], v133 offset:42688
	ds_read_b128 v[104:107], v164 offset:33920
	ds_read_b128 v[164:167], v164 offset:33984
	s_waitcnt lgkmcnt(7)
	v_mfma_f32_16x16x32_bf16 v[76:79], v[84:87], v[8:11], v[76:79]
	s_waitcnt lgkmcnt(5)
	v_mfma_f32_16x16x32_bf16 v[88:91], v[92:95], v[8:11], v[88:91]
	s_waitcnt lgkmcnt(3)
	v_mfma_f32_16x16x32_bf16 v[96:99], v[100:103], v[8:11], v[96:99]
	s_waitcnt lgkmcnt(1)
	v_mfma_f32_16x16x32_bf16 v[168:171], v[104:107], v[8:11], v[108:111]
	v_mfma_f32_16x16x32_bf16 v[112:115], v[84:87], v[24:27], v[112:115]
	v_mfma_f32_16x16x32_bf16 v[172:175], v[92:95], v[24:27], v[116:119]
	v_mfma_f32_16x16x32_bf16 v[176:179], v[100:103], v[24:27], v[120:123]
	v_mfma_f32_16x16x32_bf16 v[194:197], v[104:107], v[24:27], v[124:127]
	v_mfma_f32_16x16x32_bf16 v[136:139], v[84:87], v[40:43], v[136:139]
	v_mfma_f32_16x16x32_bf16 v[140:143], v[92:95], v[40:43], v[140:143]
	v_mfma_f32_16x16x32_bf16 v[144:147], v[100:103], v[40:43], v[144:147]
	v_mfma_f32_16x16x32_bf16 v[148:151], v[104:107], v[40:43], v[148:151]
	v_mfma_f32_16x16x32_bf16 v[64:67], v[84:87], v[56:59], v[64:67]
	v_mfma_f32_16x16x32_bf16 v[198:201], v[92:95], v[56:59], v[68:71]
	v_mfma_f32_16x16x32_bf16 v[72:75], v[100:103], v[56:59], v[72:75]
	v_mfma_f32_16x16x32_bf16 v[202:205], v[104:107], v[56:59], v[80:83]
	v_mfma_f32_16x16x32_bf16 v[124:127], v[152:155], v[12:15], v[76:79]
	v_mfma_f32_16x16x32_bf16 v[116:119], v[156:159], v[12:15], v[88:91]
	v_mfma_f32_16x16x32_bf16 v[108:111], v[160:163], v[12:15], v[96:99]
	s_waitcnt lgkmcnt(0)
	v_mfma_f32_16x16x32_bf16 v[100:103], v[164:167], v[12:15], v[168:171]
	v_mfma_f32_16x16x32_bf16 v[120:123], v[152:155], v[28:31], v[112:115]
	v_mfma_f32_16x16x32_bf16 v[112:115], v[156:159], v[28:31], v[172:175]
	v_mfma_f32_16x16x32_bf16 v[104:107], v[160:163], v[28:31], v[176:179]
	v_mfma_f32_16x16x32_bf16 v[96:99], v[164:167], v[28:31], v[194:197]
	v_mfma_f32_16x16x32_bf16 v[92:95], v[152:155], v[44:47], v[136:139]
	v_mfma_f32_16x16x32_bf16 v[84:87], v[156:159], v[44:47], v[140:143]
	s_nop 1
	v_xor_b32_e32 v138, 0x80000000, v131
	v_mfma_f32_16x16x32_bf16 v[76:79], v[160:163], v[44:47], v[144:147]
	v_mfma_f32_16x16x32_bf16 v[68:71], v[164:167], v[44:47], v[148:151]
	v_mfma_f32_16x16x32_bf16 v[88:91], v[152:155], v[60:63], v[64:67]
	v_mfma_f32_16x16x32_bf16 v[80:83], v[156:159], v[60:63], v[198:201]
	v_mfma_f32_16x16x32_bf16 v[72:75], v[160:163], v[60:63], v[72:75]
	v_mfma_f32_16x16x32_bf16 v[64:67], v[164:167], v[60:63], v[202:205]
	s_and_saveexec_b64 s[4:5], vcc
	s_cbranch_execz .LBB0_305
; template <bool FINAL>
; __device__ __forceinline__ void lru_unit(const Args& a, unsigned char* lds_g, int b, int cidx, int blk, int tid, bf16x8_t (&wl)[2][2][4], int& wl_blk) {
;     ...
;     for (int d = 0; d < 2; ++d) {
;         const float ba = gba[d], bx = gbx[d], lam = glam[d];
;         const float sp = (-lam > 20.f) ? -lam : log1pf(__expf(-lam));
	v_mul_f32_e32 v131, 0xbfb8aa3b, v131
	v_exp_f32_e32 v133, v131
	s_nop 0
	v_add_f32_e32 v131, 1.0, v133
	v_frexp_mant_f32_e32 v139, v131
	v_cvt_f64_f32_e32 v[136:137], v131
	v_add_f32_e32 v138, -1.0, v131
	v_frexp_exp_i32_f64_e32 v136, v[136:137]
	v_cmp_gt_f32_e32 vcc, s36, v139
	v_sub_f32_e32 v140, v138, v131
	v_sub_f32_e32 v138, v133, v138
	v_subbrev_co_u32_e32 v144, vcc, 0, v136, vcc
	v_add_f32_e32 v140, 1.0, v140
	v_sub_u32_e32 v136, 0, v144
	v_add_f32_e32 v138, v138, v140
	v_ldexp_f32 v131, v131, v136
	v_ldexp_f32 v136, v138, v136
	v_add_f32_e32 v138, -1.0, v131
	v_add_f32_e32 v137, 1.0, v138
	v_sub_f32_e32 v137, v131, v137
	v_add_f32_e32 v139, v136, v137
	v_add_f32_e32 v137, 1.0, v131
	v_add_f32_e32 v140, -1.0, v137
	v_sub_f32_e32 v131, v131, v140
	v_add_f32_e32 v131, v136, v131
	v_add_f32_e32 v145, v137, v131
	v_rcp_f32_e32 v146, v145
	v_sub_f32_e32 v136, v145, v137
	v_add_f32_e32 v137, v138, v139
	v_sub_f32_e32 v131, v131, v136
	v_mul_f32_e32 v148, v137, v146
	v_sub_f32_e32 v136, v137, v138
	v_mul_f32_e32 v138, v145, v148
	v_fma_f32 v140, v148, v145, -v138
	v_fmac_f32_e32 v140, v148, v131
	v_sub_f32_e32 v147, v139, v136
	v_add_f32_e32 v136, v138, v140
	v_sub_f32_e32 v139, v137, v136
	v_pk_add_f32 v[142:143], v[136:137], v[138:139] neg_lo:[0,1] neg_hi:[0,1]
	v_mov_b32_e32 v141, v136
	v_pk_add_f32 v[136:137], v[142:143], v[140:141] neg_lo:[0,1] neg_hi:[0,1]
	v_cmp_neq_f32_e32 vcc, s38, v133
	v_add_f32_e32 v137, v147, v137
	v_add_f32_e32 v136, v136, v137
	v_add_f32_e32 v137, v139, v136
	v_mul_f32_e32 v147, v146, v137
	v_mul_f32_e32 v138, v145, v147
	v_fma_f32 v140, v147, v145, -v138
	v_fmac_f32_e32 v140, v147, v131
	v_sub_f32_e32 v131, v139, v137
	v_add_f32_e32 v131, v136, v131
	v_add_f32_e32 v136, v138, v140
	v_sub_f32_e32 v139, v137, v136
	v_pk_add_f32 v[142:143], v[136:137], v[138:139] neg_lo:[0,1] neg_hi:[0,1]
	v_mov_b32_e32 v141, v136
	v_pk_add_f32 v[136:137], v[142:143], v[140:141] neg_lo:[0,1] neg_hi:[0,1]
	s_nop 0
	v_add_f32_e32 v131, v131, v137
	v_add_f32_e32 v131, v136, v131
	v_add_f32_e32 v137, v148, v147
	v_add_f32_e32 v131, v139, v131
	v_sub_f32_e32 v136, v137, v148
	v_mul_f32_e32 v131, v146, v131
	v_sub_f32_e32 v136, v147, v136
	v_add_f32_e32 v138, v136, v131
	v_add_f32_e32 v140, v137, v138
	v_cvt_f32_i32_e32 v136, v144
	v_mul_f32_e32 v141, v140, v140
	v_sub_f32_e32 v137, v140, v137
	v_fmamk_f32 v131, v141, 0x3e9b6dac, v181
	v_sub_f32_e32 v137, v138, v137
	v_fmaak_f32 v131, v141, v131, 0x3f2aaada
	v_ldexp_f32 v142, v137, 1
	v_mul_f32_e32 v137, v140, v141
	v_ldexp_f32 v139, v140, 1
	v_pk_mul_f32 v[140:141], v[136:137], v[130:131]
	s_nop 0
	v_fma_f32 v138, v136, s37, -v140
	v_fmac_f32_e32 v138, 0xb102e308, v136
	v_pk_add_f32 v[136:137], v[140:141], v[138:139]
	s_nop 0
	v_sub_f32_e32 v131, v137, v139
	v_sub_f32_e32 v131, v141, v131
	v_add_f32_e32 v143, v142, v131
	v_mov_b32_e32 v142, v140
	v_pk_add_f32 v[140:141], v[136:137], v[140:141] neg_lo:[0,1] neg_hi:[0,1]
	v_pk_add_f32 v[144:145], v[136:137], v[142:143]
	v_mov_b32_e32 v139, v136
	v_mov_b32_e32 v141, v145
	v_pk_add_f32 v[146:147], v[138:139], v[140:141] neg_lo:[0,1] neg_hi:[0,1]
	v_pk_add_f32 v[138:139], v[138:139], v[140:141]
	v_mov_b32_e32 v142, v143
	v_pk_add_f32 v[140:141], v[138:139], v[136:137] op_sel:[1,0] op_sel_hi:[0,1] neg_lo:[0,1] neg_hi:[0,1]
	v_pk_add_f32 v[148:149], v[144:145], v[140:141] op_sel_hi:[1,0] neg_lo:[0,1] neg_hi:[0,1]
	v_mov_b32_e32 v144, v145
	v_mov_b32_e32 v145, v139
	v_pk_mov_b32 v[140:141], v[136:137], v[140:141] op_sel:[1,0]
	v_mov_b32_e32 v143, v136
	v_pk_add_f32 v[140:141], v[144:145], v[140:141] neg_lo:[0,1] neg_hi:[0,1]
	v_mov_b32_e32 v148, v146
	v_pk_add_f32 v[136:137], v[142:143], v[140:141] neg_lo:[0,1] neg_hi:[0,1]
	v_mov_b32_e32 v147, v139
	v_pk_add_f32 v[140:141], v[148:149], v[136:137]
	s_nop 0
	v_pk_add_f32 v[142:143], v[140:141], v[140:141] op_sel:[0,1] op_sel_hi:[1,0]
	s_nop 0
	v_pk_add_f32 v[138:139], v[138:139], v[142:143] op_sel:[1,0] op_sel_hi:[0,1]
	v_mov_b32_e32 v141, v138
	v_pk_add_f32 v[144:145], v[140:141], v[146:147] neg_lo:[0,1] neg_hi:[0,1]
	v_mov_b32_e32 v137, v142
	v_sub_f32_e32 v131, v140, v144
	v_pk_add_f32 v[136:137], v[136:137], v[144:145] neg_lo:[0,1] neg_hi:[0,1]
	v_sub_f32_e32 v131, v146, v131
	v_add_f32_e32 v131, v136, v131
	v_add_f32_e32 v131, v131, v137
	v_add_f32_e32 v131, v138, v131
	v_cndmask_b32_e32 v131, v182, v131, vcc
	v_cmp_ngt_f32_e32 vcc, -1.0, v133
	s_nop 1
	v_cndmask_b32_e32 v131, v183, v131, vcc
	v_cmp_neq_f32_e32 vcc, -1.0, v133
	s_nop 1
	v_cndmask_b32_e32 v131, v184, v131, vcc
	v_cmp_lt_f32_e64 vcc, |v133|, s39
	s_nop 1
	v_cndmask_b32_e32 v138, v131, v133, vcc
